# HGRN2 pass B: fold of earlier group states software-pipelined with a second register set (on top of v16)
# baseline (speedup 1.0000x reference)
.Lfold_loop:
	s_cmp_eq_u32 s89, s66
	s_cbranch_scc1 .Lfold_tailA
	s_ashr_i32 s67, s66, 31
	s_lshl_b64 s[70:71], s[66:67], 16
	s_add_u32 s70, s3, s70
	s_addc_u32 s71, s74, s71
	v_lshl_add_u64 v[242:243], s[70:71], 0, v[78:79]
	v_add_co_u32_e32 v214, vcc, s75, v242
	s_lshl_b64 s[72:73], s[66:67], 9
	s_nop 0
	v_addc_co_u32_e32 v215, vcc, 0, v243, vcc
	v_add_co_u32_e32 v218, vcc, s76, v242
	v_lshl_add_u64 v[206:207], v[66:67], 0, s[72:73]
	s_nop 0
	v_addc_co_u32_e32 v219, vcc, 0, v243, vcc
	v_add_co_u32_e32 v222, vcc, s77, v242
	global_load_dwordx4 v[206:209], v[206:207], off
	s_nop 0
	v_addc_co_u32_e32 v223, vcc, 0, v243, vcc
	v_add_co_u32_e32 v226, vcc, s78, v242
	global_load_dwordx4 v[210:213], v[242:243], off
	s_nop 0
	global_load_dwordx4 v[214:217], v[214:215], off
	v_addc_co_u32_e32 v227, vcc, 0, v243, vcc
	v_add_co_u32_e32 v230, vcc, s79, v242
	global_load_dwordx4 v[218:221], v[218:219], off
	s_nop 0
	global_load_dwordx4 v[222:225], v[222:223], off
	v_addc_co_u32_e32 v231, vcc, 0, v243, vcc
	v_add_co_u32_e32 v234, vcc, s80, v242
	global_load_dwordx4 v[226:229], v[226:227], off
	s_nop 0
	global_load_dwordx4 v[230:233], v[230:231], off
	v_addc_co_u32_e32 v235, vcc, 0, v243, vcc
	v_add_co_u32_e32 v242, vcc, s81, v242
	global_load_dwordx4 v[234:237], v[234:235], off
	s_nop 0
	v_addc_co_u32_e32 v243, vcc, 0, v243, vcc
	global_load_dwordx4 v[238:241], v[242:243], off
	s_add_i32 s66, s66, 1
	s_waitcnt vmcnt(17)
	v_mul_f32_e32 v34, 0x3fb8aa3b, v34
	v_mul_f32_e32 v35, 0x3fb8aa3b, v35
	v_mul_f32_e32 v36, 0x3fb8aa3b, v36
	v_mul_f32_e32 v37, 0x3fb8aa3b, v37
	v_exp_f32_e32 v34, v34
	v_exp_f32_e32 v36, v36
	v_exp_f32_e32 v37, v37
	v_exp_f32_e32 v35, v35
	s_waitcnt vmcnt(16)
	v_pk_fma_f32 v[8:9], v[8:9], v[36:37], v[40:41]
	v_pk_fma_f32 v[6:7], v[6:7], v[34:35], v[38:39]
	s_waitcnt vmcnt(15)
	v_pk_fma_f32 v[20:21], v[20:21], v[36:37], v[44:45]
	v_pk_fma_f32 v[18:19], v[18:19], v[34:35], v[42:43]
	s_waitcnt vmcnt(14)
	v_pk_fma_f32 v[24:25], v[24:25], v[36:37], v[48:49]
	v_pk_fma_f32 v[22:23], v[22:23], v[34:35], v[46:47]
	s_waitcnt vmcnt(13)
	v_pk_fma_f32 v[32:33], v[32:33], v[36:37], v[52:53]
	v_pk_fma_f32 v[30:31], v[30:31], v[34:35], v[50:51]
	s_waitcnt vmcnt(12)
	v_pk_fma_f32 v[28:29], v[28:29], v[36:37], v[56:57]
	v_pk_fma_f32 v[26:27], v[26:27], v[34:35], v[54:55]
	s_waitcnt vmcnt(11)
	v_pk_fma_f32 v[16:17], v[16:17], v[36:37], v[60:61]
	v_pk_fma_f32 v[14:15], v[14:15], v[34:35], v[58:59]
	s_waitcnt vmcnt(10)
	v_pk_fma_f32 v[12:13], v[12:13], v[36:37], v[82:83]
	v_pk_fma_f32 v[10:11], v[10:11], v[34:35], v[80:81]
	s_waitcnt vmcnt(9)
	v_pk_fma_f32 v[4:5], v[4:5], v[36:37], v[86:87]
	v_pk_fma_f32 v[2:3], v[2:3], v[34:35], v[84:85]
	s_cmp_eq_u32 s89, s66
	s_cbranch_scc1 .Lfold_tailB
	s_ashr_i32 s67, s66, 31
	s_lshl_b64 s[70:71], s[66:67], 16
	s_add_u32 s70, s3, s70
	s_addc_u32 s71, s74, s71
	v_lshl_add_u64 v[62:63], s[70:71], 0, v[78:79]
	v_add_co_u32_e32 v42, vcc, s75, v62
	s_lshl_b64 s[72:73], s[66:67], 9
	s_nop 0
	v_addc_co_u32_e32 v43, vcc, 0, v63, vcc
	v_add_co_u32_e32 v46, vcc, s76, v62
	v_lshl_add_u64 v[34:35], v[66:67], 0, s[72:73]
	s_nop 0
	v_addc_co_u32_e32 v47, vcc, 0, v63, vcc
	v_add_co_u32_e32 v50, vcc, s77, v62
	global_load_dwordx4 v[34:37], v[34:35], off
	s_nop 0
	v_addc_co_u32_e32 v51, vcc, 0, v63, vcc
	v_add_co_u32_e32 v54, vcc, s78, v62
	global_load_dwordx4 v[38:41], v[62:63], off
	s_nop 0
	global_load_dwordx4 v[42:45], v[42:43], off
	v_addc_co_u32_e32 v55, vcc, 0, v63, vcc
	v_add_co_u32_e32 v58, vcc, s79, v62
	global_load_dwordx4 v[46:49], v[46:47], off
	s_nop 0
	global_load_dwordx4 v[50:53], v[50:51], off
	v_addc_co_u32_e32 v59, vcc, 0, v63, vcc
	v_add_co_u32_e32 v80, vcc, s80, v62
	global_load_dwordx4 v[54:57], v[54:55], off
	s_nop 0
	global_load_dwordx4 v[58:61], v[58:59], off
	v_addc_co_u32_e32 v81, vcc, 0, v63, vcc
	v_add_co_u32_e32 v62, vcc, s81, v62
	global_load_dwordx4 v[80:83], v[80:81], off
	s_nop 0
	v_addc_co_u32_e32 v63, vcc, 0, v63, vcc
	global_load_dwordx4 v[84:87], v[62:63], off
	s_add_i32 s66, s66, 1
	s_waitcnt vmcnt(17)
	v_mul_f32_e32 v206, 0x3fb8aa3b, v206
	v_mul_f32_e32 v207, 0x3fb8aa3b, v207
	v_mul_f32_e32 v208, 0x3fb8aa3b, v208
	v_mul_f32_e32 v209, 0x3fb8aa3b, v209
	v_exp_f32_e32 v206, v206
	v_exp_f32_e32 v208, v208
	v_exp_f32_e32 v209, v209
	v_exp_f32_e32 v207, v207
	s_waitcnt vmcnt(16)
	v_pk_fma_f32 v[8:9], v[8:9], v[208:209], v[212:213]
	v_pk_fma_f32 v[6:7], v[6:7], v[206:207], v[210:211]
	s_waitcnt vmcnt(15)
	v_pk_fma_f32 v[20:21], v[20:21], v[208:209], v[216:217]
	v_pk_fma_f32 v[18:19], v[18:19], v[206:207], v[214:215]
	s_waitcnt vmcnt(14)
	v_pk_fma_f32 v[24:25], v[24:25], v[208:209], v[220:221]
	v_pk_fma_f32 v[22:23], v[22:23], v[206:207], v[218:219]
	s_waitcnt vmcnt(13)
	v_pk_fma_f32 v[32:33], v[32:33], v[208:209], v[224:225]
	v_pk_fma_f32 v[30:31], v[30:31], v[206:207], v[222:223]
	s_waitcnt vmcnt(12)
	v_pk_fma_f32 v[28:29], v[28:29], v[208:209], v[228:229]
	v_pk_fma_f32 v[26:27], v[26:27], v[206:207], v[226:227]
	s_waitcnt vmcnt(11)
	v_pk_fma_f32 v[16:17], v[16:17], v[208:209], v[232:233]
	v_pk_fma_f32 v[14:15], v[14:15], v[206:207], v[230:231]
	s_waitcnt vmcnt(10)
	v_pk_fma_f32 v[12:13], v[12:13], v[208:209], v[236:237]
	v_pk_fma_f32 v[10:11], v[10:11], v[206:207], v[234:235]
	s_waitcnt vmcnt(9)
	v_pk_fma_f32 v[4:5], v[4:5], v[208:209], v[240:241]
	v_pk_fma_f32 v[2:3], v[2:3], v[206:207], v[238:239]
	s_branch .Lfold_loop
.Lfold_tailA:
	s_waitcnt vmcnt(8)
	v_mul_f32_e32 v34, 0x3fb8aa3b, v34
	v_mul_f32_e32 v35, 0x3fb8aa3b, v35
	v_mul_f32_e32 v36, 0x3fb8aa3b, v36
	v_mul_f32_e32 v37, 0x3fb8aa3b, v37
	v_exp_f32_e32 v34, v34
	v_exp_f32_e32 v36, v36
	v_exp_f32_e32 v37, v37
	v_exp_f32_e32 v35, v35
	s_waitcnt vmcnt(7)
	v_pk_fma_f32 v[8:9], v[8:9], v[36:37], v[40:41]
	v_pk_fma_f32 v[6:7], v[6:7], v[34:35], v[38:39]
	s_waitcnt vmcnt(6)
	v_pk_fma_f32 v[20:21], v[20:21], v[36:37], v[44:45]
	v_pk_fma_f32 v[18:19], v[18:19], v[34:35], v[42:43]
	s_waitcnt vmcnt(5)
	v_pk_fma_f32 v[24:25], v[24:25], v[36:37], v[48:49]
	v_pk_fma_f32 v[22:23], v[22:23], v[34:35], v[46:47]
	s_waitcnt vmcnt(4)
	v_pk_fma_f32 v[32:33], v[32:33], v[36:37], v[52:53]
	v_pk_fma_f32 v[30:31], v[30:31], v[34:35], v[50:51]
	s_waitcnt vmcnt(3)
	v_pk_fma_f32 v[28:29], v[28:29], v[36:37], v[56:57]
	v_pk_fma_f32 v[26:27], v[26:27], v[34:35], v[54:55]
	s_waitcnt vmcnt(2)
	v_pk_fma_f32 v[16:17], v[16:17], v[36:37], v[60:61]
	v_pk_fma_f32 v[14:15], v[14:15], v[34:35], v[58:59]
	s_waitcnt vmcnt(1)
	v_pk_fma_f32 v[12:13], v[12:13], v[36:37], v[82:83]
	v_pk_fma_f32 v[10:11], v[10:11], v[34:35], v[80:81]
	s_waitcnt vmcnt(0)
	v_pk_fma_f32 v[4:5], v[4:5], v[36:37], v[86:87]
	v_pk_fma_f32 v[2:3], v[2:3], v[34:35], v[84:85]
	s_branch .LBB0_1454
.Lfold_tailB:
	s_waitcnt vmcnt(8)
	v_mul_f32_e32 v206, 0x3fb8aa3b, v206
	v_mul_f32_e32 v207, 0x3fb8aa3b, v207
	v_mul_f32_e32 v208, 0x3fb8aa3b, v208
	v_mul_f32_e32 v209, 0x3fb8aa3b, v209
	v_exp_f32_e32 v206, v206
	v_exp_f32_e32 v208, v208
	v_exp_f32_e32 v209, v209
	v_exp_f32_e32 v207, v207
	s_waitcnt vmcnt(7)
	v_pk_fma_f32 v[8:9], v[8:9], v[208:209], v[212:213]
	v_pk_fma_f32 v[6:7], v[6:7], v[206:207], v[210:211]
	s_waitcnt vmcnt(6)
	v_pk_fma_f32 v[20:21], v[20:21], v[208:209], v[216:217]
	v_pk_fma_f32 v[18:19], v[18:19], v[206:207], v[214:215]
	s_waitcnt vmcnt(5)
	v_pk_fma_f32 v[24:25], v[24:25], v[208:209], v[220:221]
	v_pk_fma_f32 v[22:23], v[22:23], v[206:207], v[218:219]
	s_waitcnt vmcnt(4)
	v_pk_fma_f32 v[32:33], v[32:33], v[208:209], v[224:225]
	v_pk_fma_f32 v[30:31], v[30:31], v[206:207], v[222:223]
	s_waitcnt vmcnt(3)
	v_pk_fma_f32 v[28:29], v[28:29], v[208:209], v[228:229]
	v_pk_fma_f32 v[26:27], v[26:27], v[206:207], v[226:227]
	s_waitcnt vmcnt(2)
	v_pk_fma_f32 v[16:17], v[16:17], v[208:209], v[232:233]
	v_pk_fma_f32 v[14:15], v[14:15], v[206:207], v[230:231]
	s_waitcnt vmcnt(1)
	v_pk_fma_f32 v[12:13], v[12:13], v[208:209], v[236:237]
	v_pk_fma_f32 v[10:11], v[10:11], v[206:207], v[234:235]
	s_waitcnt vmcnt(0)
	v_pk_fma_f32 v[4:5], v[4:5], v[208:209], v[240:241]
	v_pk_fma_f32 v[2:3], v[2:3], v[206:207], v[238:239]
